# J1 + in-proj epilogue row sum-of-squares: cross-lane sums via v_permlane16_swap/v_permlane32_swap instead of ds_bpermute_b32 (32 more sites)
# baseline (speedup 1.0000x reference)
.LBB0_289:
	s_lshl_b32 s6, s9, 8
	s_add_i32 s9, s6, s48
	s_lshl_b32 s6, s8, 8
	s_or_b32 s64, s6, s49
	s_cmp_lt_i32 s8, 4
	s_cselect_b64 s[26:27], -1, 0
	s_lshl_b32 s6, s8, 2
	s_ashr_i32 s7, s6, 31
	s_lshl_b64 s[6:7], s[6:7], 2
	v_mbcnt_lo_u32_b32 v135, -1, 0
	v_mbcnt_hi_u32_b32 v135, -1, v135
	s_add_u32 s14, s51, s6
	v_ashrrev_i32_e32 v132, 1, v135
	v_and_b32_e32 v132, -8, v132
	s_addc_u32 s15, s56, s7
	v_and_or_b32 v134, v135, 15, s9
	v_add_u32_e32 v132, s64, v132
	v_mov_b64_e32 v[146:147], s[22:23]
	s_cmp_gt_i32 s8, 3
	v_ashrrev_i32_e32 v133, 31, v132
	v_mad_i64_i32 v[146:147], s[8:9], v134, s59, v[146:147]
	v_cmp_gt_u32_e64 s[6:7], 16, v135
	v_ashrrev_i32_e32 v135, 31, v134
	v_lshl_add_u64 v[150:151], v[132:133], 1, v[146:147]
	v_cvt_pk_bf16_f32 v146, v124, v125
	v_cvt_pk_bf16_f32 v147, v126, v127
	v_cvt_pk_bf16_f32 v148, v120, v121
	v_cvt_pk_bf16_f32 v149, v122, v123
	global_store_dwordx4 v[150:151], v[146:149], off
	s_nop 1
	v_cvt_pk_bf16_f32 v146, v116, v117
	v_cvt_pk_bf16_f32 v147, v118, v119
	v_cvt_pk_bf16_f32 v148, v112, v113
	v_cvt_pk_bf16_f32 v149, v114, v115
	global_store_dwordx4 v[150:151], v[146:149], off offset:256
	s_cbranch_scc1 .LBB0_293
	v_mul_f32_e32 v115, v115, v115
	v_fmac_f32_e32 v115, v114, v114
	v_mul_f32_e32 v114, v117, v117
	v_mul_f32_e32 v123, v123, v123
	v_fmac_f32_e32 v114, v116, v116
	v_mul_f32_e32 v116, v119, v119
	v_fmac_f32_e32 v123, v122, v122
	v_mul_f32_e32 v122, v125, v125
	v_fmac_f32_e32 v116, v118, v118
	v_mul_f32_e32 v113, v113, v113
	v_fmac_f32_e32 v122, v124, v124
	v_mul_f32_e32 v124, v127, v127
	v_add_f32_e32 v114, v114, v116
	v_fmac_f32_e32 v113, v112, v112
	v_fmac_f32_e32 v124, v126, v126
	v_mul_f32_e32 v121, v121, v121
	v_add_f32_e32 v112, v114, v113
	v_and_b32_e32 v114, 64, v145
	v_add_f32_e32 v122, v122, v124
	v_fmac_f32_e32 v121, v120, v120
	v_xor_b32_e32 v113, 16, v145
	v_add_u32_e32 v114, 64, v114
	v_add_f32_e32 v120, v122, v121
	v_cmp_lt_i32_e32 vcc, v113, v114
	v_add_f32_e32 v120, v123, v120
	v_add_f32_e32 v112, v115, v112
	v_cndmask_b32_e32 v113, v145, v113, vcc
	v_add_f32_e32 v112, v120, v112
	v_lshlrev_b32_e32 v113, 2, v113
	v_mov_b32_e32 v113, v112
	s_nop 1
	v_permlane16_swap_b32_e32 v113, v112
	s_waitcnt lgkmcnt(0)
	v_add_f32_e32 v112, v112, v113
	v_xor_b32_e32 v113, 32, v145
	v_cmp_lt_i32_e32 vcc, v113, v114
	s_nop 1
	v_cndmask_b32_e32 v113, v145, v113, vcc
	v_lshlrev_b32_e32 v113, 2, v113
	v_mov_b32_e32 v113, v112
	s_nop 1
	v_permlane32_swap_b32_e32 v113, v112
	s_and_saveexec_b64 s[8:9], s[6:7]
	s_cbranch_execz .LBB0_292
	v_lshlrev_b64 v[114:115], 6, v[134:135]
	v_lshl_add_u64 v[114:115], s[14:15], 0, v[114:115]
	s_waitcnt lgkmcnt(0)
	v_add_f32_e32 v112, v112, v113
	global_store_dword v[114:115], v112, off

.LBB0_293:
	v_or_b32_e32 v112, 16, v134
	v_mov_b64_e32 v[114:115], s[22:23]
	v_mad_i64_i32 v[114:115], s[8:9], v112, s59, v[114:115]
	s_waitcnt lgkmcnt(0)
	v_cndmask_b32_e64 v113, 0, 1, s[26:27]
	v_lshl_add_u64 v[118:119], v[132:133], 1, v[114:115]
	v_cvt_pk_bf16_f32 v114, v108, v109
	v_cvt_pk_bf16_f32 v115, v110, v111
	v_cvt_pk_bf16_f32 v116, v104, v105
	v_cvt_pk_bf16_f32 v117, v106, v107
	v_cmp_ne_u32_e64 s[8:9], 1, v113
	s_andn2_b64 vcc, exec, s[26:27]
	global_store_dwordx4 v[118:119], v[114:117], off
	s_nop 1
	v_cvt_pk_bf16_f32 v114, v100, v101
	v_cvt_pk_bf16_f32 v115, v102, v103
	v_cvt_pk_bf16_f32 v116, v96, v97
	v_cvt_pk_bf16_f32 v117, v98, v99
	global_store_dwordx4 v[118:119], v[114:117], off offset:256
	s_cbranch_vccnz .LBB0_297
	v_mul_f32_e32 v99, v99, v99
	v_fmac_f32_e32 v99, v98, v98
	v_mul_f32_e32 v98, v101, v101
	v_mul_f32_e32 v107, v107, v107
	v_fmac_f32_e32 v98, v100, v100
	v_mul_f32_e32 v100, v103, v103
	v_fmac_f32_e32 v107, v106, v106
	v_mul_f32_e32 v106, v109, v109
	v_fmac_f32_e32 v100, v102, v102
	v_mul_f32_e32 v97, v97, v97
	v_fmac_f32_e32 v106, v108, v108
	v_mul_f32_e32 v108, v111, v111
	v_add_f32_e32 v98, v98, v100
	v_fmac_f32_e32 v97, v96, v96
	v_fmac_f32_e32 v108, v110, v110
	v_mul_f32_e32 v105, v105, v105
	v_add_f32_e32 v96, v98, v97
	v_and_b32_e32 v98, 64, v145
	v_add_f32_e32 v106, v106, v108
	v_fmac_f32_e32 v105, v104, v104
	v_xor_b32_e32 v97, 16, v145
	v_add_u32_e32 v98, 64, v98
	v_add_f32_e32 v104, v106, v105
	v_cmp_lt_i32_e32 vcc, v97, v98
	v_add_f32_e32 v104, v107, v104
	v_add_f32_e32 v96, v99, v96
	v_cndmask_b32_e32 v97, v145, v97, vcc
	v_add_f32_e32 v96, v104, v96
	v_lshlrev_b32_e32 v97, 2, v97
	v_mov_b32_e32 v97, v96
	s_nop 1
	v_permlane16_swap_b32_e32 v97, v96
	s_waitcnt lgkmcnt(0)
	v_add_f32_e32 v96, v96, v97
	v_xor_b32_e32 v97, 32, v145
	v_cmp_lt_i32_e32 vcc, v97, v98
	s_nop 1
	v_cndmask_b32_e32 v97, v145, v97, vcc
	v_lshlrev_b32_e32 v97, 2, v97
	v_mov_b32_e32 v97, v96
	s_nop 1
	v_permlane32_swap_b32_e32 v97, v96
	s_and_saveexec_b64 s[26:27], s[6:7]
	s_cbranch_execz .LBB0_296
	v_ashrrev_i32_e32 v113, 31, v112
	v_lshlrev_b64 v[98:99], 6, v[112:113]
	v_lshl_add_u64 v[98:99], s[14:15], 0, v[98:99]
	s_waitcnt lgkmcnt(0)
	v_add_f32_e32 v96, v96, v97
	global_store_dword v[98:99], v96, off

.LBB0_297:
	v_or_b32_e32 v96, 32, v134
	v_mov_b64_e32 v[98:99], s[22:23]
	v_mad_i64_i32 v[98:99], s[26:27], v96, s59, v[98:99]
	v_lshl_add_u64 v[102:103], v[132:133], 1, v[98:99]
	v_cvt_pk_bf16_f32 v98, v92, v93
	v_cvt_pk_bf16_f32 v99, v94, v95
	v_cvt_pk_bf16_f32 v100, v88, v89
	v_cvt_pk_bf16_f32 v101, v90, v91
	s_and_b64 vcc, exec, s[8:9]
	global_store_dwordx4 v[102:103], v[98:101], off
	s_nop 1
	v_cvt_pk_bf16_f32 v98, v84, v85
	v_cvt_pk_bf16_f32 v99, v86, v87
	v_cvt_pk_bf16_f32 v100, v80, v81
	v_cvt_pk_bf16_f32 v101, v82, v83
	global_store_dwordx4 v[102:103], v[98:101], off offset:256
	s_cbranch_vccnz .LBB0_301
	v_mul_f32_e32 v83, v83, v83
	v_fmac_f32_e32 v83, v82, v82
	v_mul_f32_e32 v82, v85, v85
	v_mul_f32_e32 v91, v91, v91
	v_fmac_f32_e32 v82, v84, v84
	v_mul_f32_e32 v84, v87, v87
	v_fmac_f32_e32 v91, v90, v90
	v_mul_f32_e32 v90, v93, v93
	v_fmac_f32_e32 v84, v86, v86
	v_mul_f32_e32 v81, v81, v81
	v_fmac_f32_e32 v90, v92, v92
	v_mul_f32_e32 v92, v95, v95
	v_add_f32_e32 v82, v82, v84
	v_fmac_f32_e32 v81, v80, v80
	v_fmac_f32_e32 v92, v94, v94
	v_mul_f32_e32 v89, v89, v89
	v_add_f32_e32 v80, v82, v81
	v_and_b32_e32 v82, 64, v145
	v_add_f32_e32 v90, v90, v92
	v_fmac_f32_e32 v89, v88, v88
	v_xor_b32_e32 v81, 16, v145
	v_add_u32_e32 v82, 64, v82
	v_add_f32_e32 v88, v90, v89
	v_cmp_lt_i32_e32 vcc, v81, v82
	v_add_f32_e32 v88, v91, v88
	v_add_f32_e32 v80, v83, v80
	v_cndmask_b32_e32 v81, v145, v81, vcc
	v_add_f32_e32 v80, v88, v80
	v_lshlrev_b32_e32 v81, 2, v81
	v_mov_b32_e32 v81, v80
	s_nop 1
	v_permlane16_swap_b32_e32 v81, v80
	s_waitcnt lgkmcnt(0)
	v_add_f32_e32 v80, v80, v81
	v_xor_b32_e32 v81, 32, v145
	v_cmp_lt_i32_e32 vcc, v81, v82
	s_nop 1
	v_cndmask_b32_e32 v81, v145, v81, vcc
	v_lshlrev_b32_e32 v81, 2, v81
	v_mov_b32_e32 v81, v80
	s_nop 1
	v_permlane32_swap_b32_e32 v81, v80
	s_and_saveexec_b64 s[26:27], s[6:7]
	s_cbranch_execz .LBB0_300
	v_ashrrev_i32_e32 v97, 31, v96
	v_lshlrev_b64 v[82:83], 6, v[96:97]
	v_lshl_add_u64 v[82:83], s[14:15], 0, v[82:83]
	s_waitcnt lgkmcnt(0)
	v_add_f32_e32 v80, v80, v81
	global_store_dword v[82:83], v80, off

.LBB0_301:
	v_or_b32_e32 v80, 48, v134
	v_mov_b64_e32 v[82:83], s[22:23]
	v_mad_i64_i32 v[82:83], s[26:27], v80, s59, v[82:83]
	v_lshl_add_u64 v[86:87], v[132:133], 1, v[82:83]
	v_cvt_pk_bf16_f32 v82, v76, v77
	v_cvt_pk_bf16_f32 v83, v78, v79
	v_cvt_pk_bf16_f32 v84, v72, v73
	v_cvt_pk_bf16_f32 v85, v74, v75
	s_and_b64 vcc, exec, s[8:9]
	global_store_dwordx4 v[86:87], v[82:85], off
	s_nop 1
	v_cvt_pk_bf16_f32 v82, v68, v69
	v_cvt_pk_bf16_f32 v83, v70, v71
	v_cvt_pk_bf16_f32 v84, v64, v65
	v_cvt_pk_bf16_f32 v85, v66, v67
	global_store_dwordx4 v[86:87], v[82:85], off offset:256
	s_cbranch_vccnz .LBB0_305
	v_mul_f32_e32 v67, v67, v67
	v_fmac_f32_e32 v67, v66, v66
	v_mul_f32_e32 v66, v69, v69
	v_mul_f32_e32 v75, v75, v75
	v_fmac_f32_e32 v66, v68, v68
	v_mul_f32_e32 v68, v71, v71
	v_fmac_f32_e32 v75, v74, v74
	v_mul_f32_e32 v74, v77, v77
	v_fmac_f32_e32 v68, v70, v70
	v_mul_f32_e32 v65, v65, v65
	v_fmac_f32_e32 v74, v76, v76
	v_mul_f32_e32 v76, v79, v79
	v_add_f32_e32 v66, v66, v68
	v_fmac_f32_e32 v65, v64, v64
	v_fmac_f32_e32 v76, v78, v78
	v_mul_f32_e32 v73, v73, v73
	v_add_f32_e32 v64, v66, v65
	v_and_b32_e32 v66, 64, v145
	v_add_f32_e32 v74, v74, v76
	v_fmac_f32_e32 v73, v72, v72
	v_xor_b32_e32 v65, 16, v145
	v_add_u32_e32 v66, 64, v66
	v_add_f32_e32 v72, v74, v73
	v_cmp_lt_i32_e32 vcc, v65, v66
	v_add_f32_e32 v72, v75, v72
	v_add_f32_e32 v64, v67, v64
	v_cndmask_b32_e32 v65, v145, v65, vcc
	v_add_f32_e32 v64, v72, v64
	v_lshlrev_b32_e32 v65, 2, v65
	v_mov_b32_e32 v65, v64
	s_nop 1
	v_permlane16_swap_b32_e32 v65, v64
	s_waitcnt lgkmcnt(0)
	v_add_f32_e32 v64, v64, v65
	v_xor_b32_e32 v65, 32, v145
	v_cmp_lt_i32_e32 vcc, v65, v66
	s_nop 1
	v_cndmask_b32_e32 v65, v145, v65, vcc
	v_lshlrev_b32_e32 v65, 2, v65
	v_mov_b32_e32 v65, v64
	s_nop 1
	v_permlane32_swap_b32_e32 v65, v64
	s_and_saveexec_b64 s[26:27], s[6:7]
	s_cbranch_execz .LBB0_304
	v_ashrrev_i32_e32 v81, 31, v80
	v_lshlrev_b64 v[66:67], 6, v[80:81]
	v_lshl_add_u64 v[66:67], s[14:15], 0, v[66:67]
	s_waitcnt lgkmcnt(0)
	v_add_f32_e32 v64, v64, v65
	global_store_dword v[66:67], v64, off

.LBB0_305:
	v_add_u32_e32 v64, 0x80, v134
	v_mov_b64_e32 v[66:67], s[22:23]
	v_mad_i64_i32 v[66:67], s[26:27], v64, s59, v[66:67]
	v_lshl_add_u64 v[70:71], v[132:133], 1, v[66:67]
	v_cvt_pk_bf16_f32 v66, v60, v61
	v_cvt_pk_bf16_f32 v67, v62, v63
	v_cvt_pk_bf16_f32 v68, v56, v57
	v_cvt_pk_bf16_f32 v69, v58, v59
	s_and_b64 vcc, exec, s[8:9]
	global_store_dwordx4 v[70:71], v[66:69], off
	s_nop 1
	v_cvt_pk_bf16_f32 v66, v52, v53
	v_cvt_pk_bf16_f32 v67, v54, v55
	v_cvt_pk_bf16_f32 v68, v48, v49
	v_cvt_pk_bf16_f32 v69, v50, v51
	global_store_dwordx4 v[70:71], v[66:69], off offset:256
	s_cbranch_vccnz .LBB0_309
	v_mul_f32_e32 v51, v51, v51
	v_fmac_f32_e32 v51, v50, v50
	v_mul_f32_e32 v50, v53, v53
	v_mul_f32_e32 v59, v59, v59
	v_fmac_f32_e32 v50, v52, v52
	v_mul_f32_e32 v52, v55, v55
	v_fmac_f32_e32 v59, v58, v58
	v_mul_f32_e32 v58, v61, v61
	v_fmac_f32_e32 v52, v54, v54
	v_mul_f32_e32 v49, v49, v49
	v_fmac_f32_e32 v58, v60, v60
	v_mul_f32_e32 v60, v63, v63
	v_add_f32_e32 v50, v50, v52
	v_fmac_f32_e32 v49, v48, v48
	v_fmac_f32_e32 v60, v62, v62
	v_mul_f32_e32 v57, v57, v57
	v_add_f32_e32 v48, v50, v49
	v_and_b32_e32 v50, 64, v145
	v_add_f32_e32 v58, v58, v60
	v_fmac_f32_e32 v57, v56, v56
	v_xor_b32_e32 v49, 16, v145
	v_add_u32_e32 v50, 64, v50
	v_add_f32_e32 v56, v58, v57
	v_cmp_lt_i32_e32 vcc, v49, v50
	v_add_f32_e32 v56, v59, v56
	v_add_f32_e32 v48, v51, v48
	v_cndmask_b32_e32 v49, v145, v49, vcc
	v_add_f32_e32 v48, v56, v48
	v_lshlrev_b32_e32 v49, 2, v49
	v_mov_b32_e32 v49, v48
	s_nop 1
	v_permlane16_swap_b32_e32 v49, v48
	s_waitcnt lgkmcnt(0)
	v_add_f32_e32 v48, v48, v49
	v_xor_b32_e32 v49, 32, v145
	v_cmp_lt_i32_e32 vcc, v49, v50
	s_nop 1
	v_cndmask_b32_e32 v49, v145, v49, vcc
	v_lshlrev_b32_e32 v49, 2, v49
	v_mov_b32_e32 v49, v48
	s_nop 1
	v_permlane32_swap_b32_e32 v49, v48
	s_and_saveexec_b64 s[26:27], s[6:7]
	s_cbranch_execz .LBB0_308
	v_ashrrev_i32_e32 v65, 31, v64
	v_lshlrev_b64 v[50:51], 6, v[64:65]
	v_lshl_add_u64 v[50:51], s[14:15], 0, v[50:51]
	s_waitcnt lgkmcnt(0)
	v_add_f32_e32 v48, v48, v49
	global_store_dword v[50:51], v48, off

.LBB0_309:
	v_add_u32_e32 v48, 0x90, v134
	v_mov_b64_e32 v[50:51], s[22:23]
	v_mad_i64_i32 v[50:51], s[26:27], v48, s59, v[50:51]
	v_lshl_add_u64 v[54:55], v[132:133], 1, v[50:51]
	v_cvt_pk_bf16_f32 v50, v44, v45
	v_cvt_pk_bf16_f32 v51, v46, v47
	v_cvt_pk_bf16_f32 v52, v40, v41
	v_cvt_pk_bf16_f32 v53, v42, v43
	s_and_b64 vcc, exec, s[8:9]
	global_store_dwordx4 v[54:55], v[50:53], off
	s_nop 1
	v_cvt_pk_bf16_f32 v50, v36, v37
	v_cvt_pk_bf16_f32 v51, v38, v39
	v_cvt_pk_bf16_f32 v52, v32, v33
	v_cvt_pk_bf16_f32 v53, v34, v35
	global_store_dwordx4 v[54:55], v[50:53], off offset:256
	s_cbranch_vccnz .LBB0_313
	v_mul_f32_e32 v35, v35, v35
	v_fmac_f32_e32 v35, v34, v34
	v_mul_f32_e32 v34, v37, v37
	v_mul_f32_e32 v43, v43, v43
	v_fmac_f32_e32 v34, v36, v36
	v_mul_f32_e32 v36, v39, v39
	v_fmac_f32_e32 v43, v42, v42
	v_mul_f32_e32 v42, v45, v45
	v_fmac_f32_e32 v36, v38, v38
	v_mul_f32_e32 v33, v33, v33
	v_fmac_f32_e32 v42, v44, v44
	v_mul_f32_e32 v44, v47, v47
	v_add_f32_e32 v34, v34, v36
	v_fmac_f32_e32 v33, v32, v32
	v_fmac_f32_e32 v44, v46, v46
	v_mul_f32_e32 v41, v41, v41
	v_add_f32_e32 v32, v34, v33
	v_and_b32_e32 v34, 64, v145
	v_add_f32_e32 v42, v42, v44
	v_fmac_f32_e32 v41, v40, v40
	v_xor_b32_e32 v33, 16, v145
	v_add_u32_e32 v34, 64, v34
	v_add_f32_e32 v40, v42, v41
	v_cmp_lt_i32_e32 vcc, v33, v34
	v_add_f32_e32 v40, v43, v40
	v_add_f32_e32 v32, v35, v32
	v_cndmask_b32_e32 v33, v145, v33, vcc
	v_add_f32_e32 v32, v40, v32
	v_lshlrev_b32_e32 v33, 2, v33
	v_mov_b32_e32 v33, v32
	s_nop 1
	v_permlane16_swap_b32_e32 v33, v32
	s_waitcnt lgkmcnt(0)
	v_add_f32_e32 v32, v32, v33
	v_xor_b32_e32 v33, 32, v145
	v_cmp_lt_i32_e32 vcc, v33, v34
	s_nop 1
	v_cndmask_b32_e32 v33, v145, v33, vcc
	v_lshlrev_b32_e32 v33, 2, v33
	v_mov_b32_e32 v33, v32
	s_nop 1
	v_permlane32_swap_b32_e32 v33, v32
	s_and_saveexec_b64 s[26:27], s[6:7]
	s_cbranch_execz .LBB0_312
	v_ashrrev_i32_e32 v49, 31, v48
	v_lshlrev_b64 v[34:35], 6, v[48:49]
	v_lshl_add_u64 v[34:35], s[14:15], 0, v[34:35]
	s_waitcnt lgkmcnt(0)
	v_add_f32_e32 v32, v32, v33
	global_store_dword v[34:35], v32, off

.LBB0_313:
	v_add_u32_e32 v32, 0xa0, v134
	v_mov_b64_e32 v[34:35], s[22:23]
	v_mad_i64_i32 v[34:35], s[26:27], v32, s59, v[34:35]
	v_lshl_add_u64 v[38:39], v[132:133], 1, v[34:35]
	v_cvt_pk_bf16_f32 v34, v28, v29
	v_cvt_pk_bf16_f32 v35, v30, v31
	v_cvt_pk_bf16_f32 v36, v24, v25
	v_cvt_pk_bf16_f32 v37, v26, v27
	s_and_b64 vcc, exec, s[8:9]
	global_store_dwordx4 v[38:39], v[34:37], off
	s_nop 1
	v_cvt_pk_bf16_f32 v34, v20, v21
	v_cvt_pk_bf16_f32 v35, v22, v23
	v_cvt_pk_bf16_f32 v36, v16, v17
	v_cvt_pk_bf16_f32 v37, v18, v19
	global_store_dwordx4 v[38:39], v[34:37], off offset:256
	s_cbranch_vccnz .LBB0_317
	v_mul_f32_e32 v19, v19, v19
	v_fmac_f32_e32 v19, v18, v18
	v_mul_f32_e32 v18, v21, v21
	v_mul_f32_e32 v27, v27, v27
	v_fmac_f32_e32 v18, v20, v20
	v_mul_f32_e32 v20, v23, v23
	v_fmac_f32_e32 v27, v26, v26
	v_mul_f32_e32 v26, v29, v29
	v_fmac_f32_e32 v20, v22, v22
	v_mul_f32_e32 v17, v17, v17
	v_fmac_f32_e32 v26, v28, v28
	v_mul_f32_e32 v28, v31, v31
	v_add_f32_e32 v18, v18, v20
	v_fmac_f32_e32 v17, v16, v16
	v_fmac_f32_e32 v28, v30, v30
	v_mul_f32_e32 v25, v25, v25
	v_add_f32_e32 v16, v18, v17
	v_and_b32_e32 v18, 64, v145
	v_add_f32_e32 v26, v26, v28
	v_fmac_f32_e32 v25, v24, v24
	v_xor_b32_e32 v17, 16, v145
	v_add_u32_e32 v18, 64, v18
	v_add_f32_e32 v24, v26, v25
	v_cmp_lt_i32_e32 vcc, v17, v18
	v_add_f32_e32 v24, v27, v24
	v_add_f32_e32 v16, v19, v16
	v_cndmask_b32_e32 v17, v145, v17, vcc
	v_add_f32_e32 v16, v24, v16
	v_lshlrev_b32_e32 v17, 2, v17
	v_mov_b32_e32 v17, v16
	s_nop 1
	v_permlane16_swap_b32_e32 v17, v16
	s_waitcnt lgkmcnt(0)
	v_add_f32_e32 v16, v16, v17
	v_xor_b32_e32 v17, 32, v145
	v_cmp_lt_i32_e32 vcc, v17, v18
	s_nop 1
	v_cndmask_b32_e32 v17, v145, v17, vcc
	v_lshlrev_b32_e32 v17, 2, v17
	v_mov_b32_e32 v17, v16
	s_nop 1
	v_permlane32_swap_b32_e32 v17, v16
	s_and_saveexec_b64 s[26:27], s[6:7]
	s_cbranch_execz .LBB0_316
	v_ashrrev_i32_e32 v33, 31, v32
	v_lshlrev_b64 v[18:19], 6, v[32:33]
	v_lshl_add_u64 v[18:19], s[14:15], 0, v[18:19]
	s_waitcnt lgkmcnt(0)
	v_add_f32_e32 v16, v16, v17
	global_store_dword v[18:19], v16, off

.LBB0_317:
	v_add_u32_e32 v16, 0xb0, v134
	v_mov_b64_e32 v[18:19], s[22:23]
	v_mad_i64_i32 v[18:19], s[26:27], v16, s59, v[18:19]
	v_lshl_add_u64 v[22:23], v[132:133], 1, v[18:19]
	v_cvt_pk_bf16_f32 v18, v12, v13
	v_cvt_pk_bf16_f32 v19, v14, v15
	v_cvt_pk_bf16_f32 v20, v8, v9
	v_cvt_pk_bf16_f32 v21, v10, v11
	s_and_b64 vcc, exec, s[8:9]
	global_store_dwordx4 v[22:23], v[18:21], off
	s_nop 1
	v_cvt_pk_bf16_f32 v18, v4, v5
	v_cvt_pk_bf16_f32 v19, v6, v7
	v_cvt_pk_bf16_f32 v20, v0, v1
	v_cvt_pk_bf16_f32 v21, v2, v3
	global_store_dwordx4 v[22:23], v[18:21], off offset:256
	s_cbranch_vccnz .LBB0_321
	v_mul_f32_e32 v3, v3, v3
	v_fmac_f32_e32 v3, v2, v2
	v_mul_f32_e32 v2, v5, v5
	v_mul_f32_e32 v11, v11, v11
	v_fmac_f32_e32 v2, v4, v4
	v_mul_f32_e32 v4, v7, v7
	v_fmac_f32_e32 v11, v10, v10
	v_mul_f32_e32 v10, v13, v13
	v_fmac_f32_e32 v4, v6, v6
	v_mul_f32_e32 v1, v1, v1
	v_fmac_f32_e32 v10, v12, v12
	v_mul_f32_e32 v12, v15, v15
	v_add_f32_e32 v2, v2, v4
	v_fmac_f32_e32 v1, v0, v0
	v_fmac_f32_e32 v12, v14, v14
	v_mul_f32_e32 v9, v9, v9
	v_add_f32_e32 v0, v2, v1
	v_and_b32_e32 v2, 64, v145
	v_add_f32_e32 v10, v10, v12
	v_fmac_f32_e32 v9, v8, v8
	v_xor_b32_e32 v1, 16, v145
	v_add_u32_e32 v2, 64, v2
	v_add_f32_e32 v8, v10, v9
	v_cmp_lt_i32_e32 vcc, v1, v2
	v_add_f32_e32 v8, v11, v8
	v_add_f32_e32 v0, v3, v0
	v_cndmask_b32_e32 v1, v145, v1, vcc
	v_add_f32_e32 v0, v8, v0
	v_lshlrev_b32_e32 v1, 2, v1
	v_mov_b32_e32 v1, v0
	s_nop 1
	v_permlane16_swap_b32_e32 v1, v0
	s_waitcnt lgkmcnt(0)
	v_add_f32_e32 v0, v0, v1
	v_xor_b32_e32 v1, 32, v145
	v_cmp_lt_i32_e32 vcc, v1, v2
	s_nop 1
	v_cndmask_b32_e32 v1, v145, v1, vcc
	v_lshlrev_b32_e32 v1, 2, v1
	v_mov_b32_e32 v1, v0
	s_nop 1
	v_permlane32_swap_b32_e32 v1, v0
	s_and_saveexec_b64 s[8:9], s[6:7]
	s_cbranch_execz .LBB0_320
	v_ashrrev_i32_e32 v17, 31, v16
	v_lshlrev_b64 v[2:3], 6, v[16:17]
	v_lshl_add_u64 v[2:3], s[14:15], 0, v[2:3]
	s_waitcnt lgkmcnt(0)
	v_add_f32_e32 v0, v0, v1
	global_store_dword v[2:3], v0, off
